# tile-level pre-test (max of both half-tile maxima vs threshold) skips both half-tile tests with one branch
# baseline (speedup 1.0000x reference)
.LBB1_23:
	v_max_f32_e32 v3, v242, v241
	v_cmp_lt_f32_e32 vcc, v244, v3
	s_cbranch_vccz .LBB1_26
	v_cmp_lt_f32_e32 vcc, v244, v242
	s_cbranch_vccz .LBB1_83
	ds_read_b128 v[10:13], v206 offset:51200
	v_sub_f32_e32 v1, v50, v236
	v_sub_f32_e32 v3, v52, v236
	v_sub_f32_e32 v5, v54, v236
	v_sub_f32_e32 v7, v56, v236
	v_exp_f32_e32 v14, v1
	v_sub_f32_e32 v1, v51, v236
	v_exp_f32_e32 v4, v3
	v_sub_f32_e32 v3, v53, v236
	v_exp_f32_e32 v6, v5
	v_sub_f32_e32 v5, v55, v236
	v_exp_f32_e32 v8, v7
	v_sub_f32_e32 v7, v57, v236
	v_exp_f32_e32 v7, v7
	v_exp_f32_e32 v5, v5
	v_exp_f32_e32 v3, v3
	v_exp_f32_e32 v1, v1
	v_cvt_pk_f16_f32 v9, v8, v7
	v_cvt_pk_f16_f32 v8, v6, v5
	v_cvt_pk_f16_f32 v7, v4, v3
	v_cvt_pk_f16_f32 v6, v14, v1
	s_waitcnt lgkmcnt(0)
	s_nop 0
	v_mfma_f32_32x32x16_f16 v[98:113], v[10:13], v[6:9], v[98:113]
	v_mfma_f32_32x32x16_f16 v[82:97], v[194:197], v[6:9], v[82:97]
	v_cmp_lt_f32_e32 vcc, v244, v241
	s_cbranch_vccz .LBB1_26

.LBB1_26:
	v_max_f32_e32 v3, v240, v239
	v_cmp_lt_f32_e32 vcc, v244, v3
	s_cbranch_vccz .LBB1_29
	v_cmp_lt_f32_e32 vcc, v244, v240
	s_cbranch_vccz .LBB1_84
	ds_read_b128 v[10:13], v206 offset:53248
	v_sub_f32_e32 v1, v34, v236
	v_sub_f32_e32 v3, v36, v236
	v_sub_f32_e32 v5, v38, v236
	v_sub_f32_e32 v7, v40, v236
	v_exp_f32_e32 v14, v1
	v_sub_f32_e32 v1, v35, v236
	v_exp_f32_e32 v4, v3
	v_sub_f32_e32 v3, v37, v236
	v_exp_f32_e32 v6, v5
	v_sub_f32_e32 v5, v39, v236
	v_exp_f32_e32 v8, v7
	v_sub_f32_e32 v7, v41, v236
	v_exp_f32_e32 v7, v7
	v_exp_f32_e32 v5, v5
	v_exp_f32_e32 v3, v3
	v_exp_f32_e32 v1, v1
	v_cvt_pk_f16_f32 v9, v8, v7
	v_cvt_pk_f16_f32 v8, v6, v5
	v_cvt_pk_f16_f32 v7, v4, v3
	v_cvt_pk_f16_f32 v6, v14, v1
	s_waitcnt lgkmcnt(0)
	s_nop 0
	v_mfma_f32_32x32x16_f16 v[98:113], v[10:13], v[6:9], v[98:113]
	v_mfma_f32_32x32x16_f16 v[82:97], v[194:197], v[6:9], v[82:97]
	v_cmp_lt_f32_e32 vcc, v244, v239
	s_cbranch_vccz .LBB1_29

.LBB1_29:
	v_max_f32_e32 v3, v238, v237
	v_cmp_lt_f32_e32 vcc, v244, v3
	s_cbranch_vccz .LBB1_32
	v_cmp_lt_f32_e32 vcc, v244, v238
	s_cbranch_vccz .LBB1_85
	ds_read_b128 v[10:13], v206 offset:55296
	v_sub_f32_e32 v1, v18, v236
	v_sub_f32_e32 v3, v20, v236
	v_sub_f32_e32 v5, v22, v236
	v_sub_f32_e32 v7, v24, v236
	v_exp_f32_e32 v14, v1
	v_sub_f32_e32 v1, v19, v236
	v_exp_f32_e32 v4, v3
	v_sub_f32_e32 v3, v21, v236
	v_exp_f32_e32 v6, v5
	v_sub_f32_e32 v5, v23, v236
	v_exp_f32_e32 v8, v7
	v_sub_f32_e32 v7, v25, v236
	v_exp_f32_e32 v7, v7
	v_exp_f32_e32 v5, v5
	v_exp_f32_e32 v3, v3
	v_exp_f32_e32 v1, v1
	v_cvt_pk_f16_f32 v9, v8, v7
	v_cvt_pk_f16_f32 v8, v6, v5
	v_cvt_pk_f16_f32 v7, v4, v3
	v_cvt_pk_f16_f32 v6, v14, v1
	s_waitcnt lgkmcnt(0)
	s_nop 0
	v_mfma_f32_32x32x16_f16 v[98:113], v[10:13], v[6:9], v[98:113]
	v_mfma_f32_32x32x16_f16 v[82:97], v[194:197], v[6:9], v[82:97]
	v_cmp_lt_f32_e32 vcc, v244, v237
	s_cbranch_vccz .LBB1_32

.LBB1_50:
	v_max_f32_e32 v3, v15, v14
	v_cmp_lt_f32_e32 vcc, v244, v3
	s_cbranch_vccz .LBB1_53
	v_cmp_lt_f32_e32 vcc, v244, v15
	s_cbranch_vccz .LBB1_87
	ds_read_b128 v[114:117], v206 offset:59392
	v_sub_f32_e32 v1, v50, v10
	v_sub_f32_e32 v3, v52, v10
	v_sub_f32_e32 v5, v54, v10
	v_sub_f32_e32 v7, v56, v10
	v_exp_f32_e32 v15, v1
	v_sub_f32_e32 v1, v51, v10
	v_exp_f32_e32 v4, v3
	v_sub_f32_e32 v3, v53, v10
	v_exp_f32_e32 v6, v5
	v_sub_f32_e32 v5, v55, v10
	v_exp_f32_e32 v8, v7
	v_sub_f32_e32 v7, v57, v10
	v_exp_f32_e32 v7, v7
	v_exp_f32_e32 v5, v5
	v_exp_f32_e32 v3, v3
	v_exp_f32_e32 v1, v1
	v_cvt_pk_f16_f32 v239, v8, v7
	v_cvt_pk_f16_f32 v238, v6, v5
	v_cvt_pk_f16_f32 v237, v4, v3
	v_cvt_pk_f16_f32 v236, v15, v1
	s_waitcnt lgkmcnt(0)
	s_nop 0
	v_mfma_f32_32x32x16_f16 v[98:113], v[114:117], v[236:239], v[98:113]
	v_mfma_f32_32x32x16_f16 v[82:97], v[194:197], v[236:239], v[82:97]
	v_cmp_lt_f32_e32 vcc, v244, v14
	s_cbranch_vccz .LBB1_53

.LBB1_53:
	v_max_f32_e32 v3, v13, v12
	v_cmp_lt_f32_e32 vcc, v244, v3
	s_cbranch_vccz .LBB1_56
	v_cmp_lt_f32_e32 vcc, v244, v13
	s_cbranch_vccz .LBB1_88
	ds_read_b128 v[14:17], v206 offset:61440
	v_sub_f32_e32 v1, v34, v10
	v_sub_f32_e32 v3, v36, v10
	v_sub_f32_e32 v5, v38, v10
	v_sub_f32_e32 v7, v40, v10
	v_exp_f32_e32 v13, v1
	v_sub_f32_e32 v1, v35, v10
	v_exp_f32_e32 v4, v3
	v_sub_f32_e32 v3, v37, v10
	v_exp_f32_e32 v6, v5
	v_sub_f32_e32 v5, v39, v10
	v_exp_f32_e32 v8, v7
	v_sub_f32_e32 v7, v41, v10
	v_exp_f32_e32 v7, v7
	v_exp_f32_e32 v5, v5
	v_exp_f32_e32 v3, v3
	v_exp_f32_e32 v1, v1
	v_cvt_pk_f16_f32 v239, v8, v7
	v_cvt_pk_f16_f32 v238, v6, v5
	v_cvt_pk_f16_f32 v237, v4, v3
	v_cvt_pk_f16_f32 v236, v13, v1
	s_waitcnt lgkmcnt(0)
	s_nop 0
	v_mfma_f32_32x32x16_f16 v[98:113], v[14:17], v[236:239], v[98:113]
	v_mfma_f32_32x32x16_f16 v[82:97], v[194:197], v[236:239], v[82:97]
	v_cmp_lt_f32_e32 vcc, v244, v12
	s_cbranch_vccz .LBB1_56

.LBB1_56:
	v_max_f32_e32 v3, v11, v9
	v_cmp_lt_f32_e32 vcc, v244, v3
	s_cbranch_vccz .LBB1_59
	v_cmp_lt_f32_e32 vcc, v244, v11
	s_cbranch_vccz .LBB1_89
	ds_read_b128 v[12:15], v206 offset:63488
	v_sub_f32_e32 v1, v18, v10
	v_sub_f32_e32 v3, v20, v10
	v_sub_f32_e32 v5, v22, v10
	v_sub_f32_e32 v7, v24, v10
	v_exp_f32_e32 v11, v1
	v_sub_f32_e32 v1, v19, v10
	v_exp_f32_e32 v4, v3
	v_sub_f32_e32 v3, v21, v10
	v_exp_f32_e32 v6, v5
	v_sub_f32_e32 v5, v23, v10
	v_exp_f32_e32 v8, v7
	v_sub_f32_e32 v7, v25, v10
	v_exp_f32_e32 v7, v7
	v_exp_f32_e32 v5, v5
	v_exp_f32_e32 v3, v3
	v_exp_f32_e32 v1, v1
	v_cvt_pk_f16_f32 v239, v8, v7
	v_cvt_pk_f16_f32 v238, v6, v5
	v_cvt_pk_f16_f32 v237, v4, v3
	v_cvt_pk_f16_f32 v236, v11, v1
	s_waitcnt lgkmcnt(0)
	s_nop 0
	v_mfma_f32_32x32x16_f16 v[98:113], v[12:15], v[236:239], v[98:113]
	v_mfma_f32_32x32x16_f16 v[82:97], v[194:197], v[236:239], v[82:97]
	v_cmp_lt_f32_e32 vcc, v244, v9
	s_cbranch_vccz .LBB1_59
